# P5 epilogue head (Lever 2): both gate pairs issued together, first 8 x loads issued before the gate waits; on top of P4a hoist + vm_wait direct branches + no-copy
# speedup vs baseline: 1.0037x; 1.0037x over previous
.LBB0_1102:
	s_ashr_i32 s3, s47, 3
	s_lshl_b32 s8, s47, 8
	v_lshl_or_b32 v192, s2, 8, v226
	s_mul_hi_i32 s9, s3, 0xc000
	s_mul_i32 s3, s3, 0xc000
	s_add_u32 s26, s74, s3
	v_ashrrev_i32_e32 v193, 31, v192
	s_addc_u32 s27, s75, s9
	v_lshlrev_b64 v[222:223], 2, v[192:193]
	v_lshl_add_u64 v[2:3], s[26:27], 0, v[222:223]
	s_mov_b64 s[26:27], 0x4000
	s_movk_i32 s3, 0x4000
	v_lshl_add_u64 v[10:11], v[2:3], 0, s[26:27]
	v_add_co_u32_e32 v2, vcc, s3, v2
	s_nop 15
	s_nop 15
	v_add_u32_e32 v210, s8, v224
	s_nop 0
	v_addc_co_u32_e32 v3, vcc, 0, v3, vcc
	global_load_dwordx4 v[2:5], v[2:3], off nt
	s_nop 0
	global_load_dwordx4 v[6:9], v[10:11], off offset:16 nt
	global_load_dwordx4 v[12:15], v[10:11], off offset:528 nt
	global_load_dwordx4 v[16:19], v[10:11], off offset:512 nt
	v_readlane_b32 s48, v254, 7
	v_readlane_b32 s49, v254, 8
	v_ashrrev_i32_e32 v211, 31, v210
	v_lshlrev_b64 v[250:251], 13, v[210:211]
	v_lshl_add_u64 v[212:213], s[48:49], 0, v[222:223]
	v_or_b32_e32 v24, 16, v210
	v_ashrrev_i32_e32 v25, 31, v24
	v_lshlrev_b64 v[218:219], 13, v[24:25]
	v_lshl_add_u64 v[20:21], v[212:213], 0, v[250:251]
	v_lshl_add_u64 v[22:23], v[212:213], 0, v[218:219]
	global_load_dwordx4 v[234:237], v[20:21], off offset:16 nt
	global_load_dwordx4 v[238:241], v[20:21], off nt
	global_load_dwordx4 v[242:245], v[20:21], off offset:528 nt
	global_load_dwordx4 v[246:249], v[20:21], off offset:512 nt
	global_load_dwordx4 v[170:173], v[22:23], off offset:16 nt
	global_load_dwordx4 v[174:177], v[22:23], off nt
	global_load_dwordx4 v[162:165], v[22:23], off offset:528 nt
	global_load_dwordx4 v[166:169], v[22:23], off offset:512 nt
	v_readlane_b32 s50, v254, 9
	v_readlane_b32 s51, v254, 10
	v_readlane_b32 s52, v254, 11
	v_readlane_b32 s53, v254, 12
	v_readlane_b32 s54, v254, 13
	v_readlane_b32 s55, v254, 14
	v_readlane_b32 s56, v254, 15
	v_readlane_b32 s57, v254, 16
	v_readlane_b32 s58, v254, 17
	v_readlane_b32 s59, v254, 18
	v_readlane_b32 s60, v254, 19
	v_readlane_b32 s61, v254, 20
	v_readlane_b32 s62, v254, 21
	v_readlane_b32 s63, v254, 22
	s_waitcnt vmcnt(10)
	v_pk_mul_f32 v[206:207], v[4:5], s[16:17] op_sel_hi:[1,0]
	v_pk_mul_f32 v[208:209], v[2:3], s[16:17] op_sel_hi:[1,0]
	v_pk_mul_f32 v[204:205], v[8:9], s[16:17] op_sel_hi:[1,0]
	v_pk_mul_f32 v[202:203], v[6:7], s[16:17] op_sel_hi:[1,0]
	s_waitcnt vmcnt(9)
	v_pk_mul_f32 v[194:195], v[12:13], s[16:17] op_sel_hi:[1,0]
	v_and_b32_e32 v3, 64, v231
	v_xor_b32_e32 v2, 16, v231
	v_add_u32_e32 v3, 64, v3
	v_cmp_lt_i32_e32 vcc, v2, v3
	s_waitcnt vmcnt(8)
	v_pk_mul_f32 v[200:201], v[16:17], s[16:17] op_sel_hi:[1,0]
	v_pk_mul_f32 v[198:199], v[18:19], s[16:17] op_sel_hi:[1,0]
	v_cndmask_b32_e32 v2, v231, v2, vcc
	v_lshlrev_b32_e32 v232, 2, v2
	v_xor_b32_e32 v2, 32, v231
	v_cmp_lt_i32_e32 vcc, v2, v3
	v_pk_mul_f32 v[196:197], v[14:15], s[16:17] op_sel_hi:[1,0]
	s_nop 0
	v_cndmask_b32_e32 v2, v231, v2, vcc
	v_lshlrev_b32_e32 v233, 2, v2
	v_or_b32_e32 v2, 32, v210
	v_ashrrev_i32_e32 v3, 31, v2
	v_lshlrev_b64 v[216:217], 13, v[2:3]
	v_lshl_add_u64 v[2:3], v[212:213], 0, v[216:217]
	global_load_dwordx4 v[26:29], v[2:3], off offset:16 nt
	global_load_dwordx4 v[30:33], v[2:3], off nt
	global_load_dwordx4 v[18:21], v[2:3], off offset:528 nt
	global_load_dwordx4 v[22:25], v[2:3], off offset:512 nt
	v_or_b32_e32 v2, 48, v210
	v_ashrrev_i32_e32 v3, 31, v2
	v_lshlrev_b64 v[214:215], 13, v[2:3]
	v_lshl_add_u64 v[6:7], v[212:213], 0, v[214:215]
	global_load_dwordx4 v[10:13], v[6:7], off offset:16 nt
	global_load_dwordx4 v[14:17], v[6:7], off nt
	global_load_dwordx4 v[2:5], v[6:7], off offset:528 nt
	s_nop 0
	global_load_dwordx4 v[6:9], v[6:7], off offset:512 nt
	v_lshl_add_u64 v[250:251], s[78:79], 0, v[250:251]
	v_lshl_add_u64 v[222:223], v[250:251], 0, v[222:223]
	s_waitcnt vmcnt(14)
	v_pk_fma_f32 v[160:161], v[160:161], v[206:207], v[240:241]
	v_pk_fma_f32 v[158:159], v[158:159], v[208:209], v[238:239]
	v_pk_fma_f32 v[154:155], v[154:155], v[202:203], v[234:235]
	s_waitcnt vmcnt(12)
	v_pk_fma_f32 v[152:153], v[152:153], v[198:199], v[248:249]
	v_pk_fma_f32 v[150:151], v[150:151], v[200:201], v[246:247]
	v_pk_fma_f32 v[146:147], v[146:147], v[194:195], v[242:243]
	v_pk_fma_f32 v[156:157], v[156:157], v[204:205], v[236:237]
	global_store_dwordx4 v[222:223], v[158:161], off
	global_store_dwordx4 v[222:223], v[154:157], off offset:16
	v_pk_fma_f32 v[148:149], v[148:149], v[196:197], v[244:245]
	v_mul_f32_e32 v159, v159, v159
	v_mul_f32_e32 v155, v155, v155
	global_store_dwordx4 v[222:223], v[150:153], off offset:512
	global_store_dwordx4 v[222:223], v[146:149], off offset:528
	v_fmac_f32_e32 v159, v158, v158
	v_mul_f32_e32 v151, v151, v151
	v_mul_f32_e32 v147, v147, v147
	v_mul_f32_e32 v158, v161, v161
	v_fmac_f32_e32 v155, v154, v154
	v_mul_f32_e32 v154, v157, v157
	v_fmac_f32_e32 v151, v150, v150
	v_mul_f32_e32 v150, v153, v153
	v_fmac_f32_e32 v147, v146, v146
	v_mul_f32_e32 v146, v149, v149
	v_fmac_f32_e32 v158, v160, v160
	v_fmac_f32_e32 v154, v156, v156
	v_fmac_f32_e32 v150, v152, v152
	v_fmac_f32_e32 v146, v148, v148
	v_add_f32_e32 v158, v159, v158
	v_add_f32_e32 v154, v155, v154
	v_add_f32_e32 v150, v151, v150
	v_add_f32_e32 v146, v147, v146
	v_add_f32_e32 v154, v158, v154
	v_add_f32_e32 v146, v150, v146
	v_add_f32_e32 v146, v154, v146
	ds_bpermute_b32 v147, v232, v146
	s_waitcnt lgkmcnt(0)
	v_add_f32_e32 v146, v146, v147
	ds_bpermute_b32 v147, v233, v146
	s_and_saveexec_b64 s[26:27], s[0:1]
	s_cbranch_execz .LBB0_1104
	s_waitcnt lgkmcnt(0)
	v_add_f32_e32 v146, v146, v147
	ds_write_b32 v227, v146
